# speedup vs baseline: 1.0025x; 1.0025x over previous
_Z8pam_mainPKDv4_jS1_S1_PKfS3_PDF16_Pf:
	s_load_dwordx8 s[4:11], s[0:1], 0x0
	s_load_dwordx4 s[12:15], s[0:1], 0x20
	s_load_dwordx2 s[16:17], s[0:1], 0x30
	v_and_b32_e32 v1, 63, v0
	v_lshrrev_b32_e32 v3, 6, v0
	v_lshlrev_b32_e32 v2, 4, v1
	v_lshlrev_b32_e32 v4, 2, v1
	v_readfirstlane_b32 s18, v3
	v_and_b32_e32 v3, 31, v1
	v_lshlrev_b32_e32 v5, 2, v3
	s_mul_i32 s19, s2, 54
	s_mul_i32 s20, s2, 3
	s_lshr_b32 s20, s20, 4
	s_mul_i32 s21, s20, 0x120
	s_sub_u32 s21, s19, s21
	s_cmp_ge_u32 s20, 24
	s_cselect_b32 s22, 0x120, 0
	s_add_u32 s22, s22, s21
	s_add_u32 s23, s20, 1
	s_cmp_ge_u32 s23, 24
	s_cselect_b32 s24, 0x120, 0
	s_sub_u32 s25, 0x120, s21
	s_cmp_lt_u32 s25, 54
	s_cselect_b32 s26, 1, 0
	s_mul_i32 s25, s25, 43
	s_lshr_b32 s25, s25, 8
	s_cmp_eq_u32 s26, 1
	s_cselect_b32 s25, s25, 100
	s_mov_b32 s29, s2
	s_mov_b32 s46, 0
	s_mov_b32 s47, 30720
	s_mov_b32 s48, 61440
	s_mov_b32 s27, 0
	s_mov_b32 s28, 1
	s_mov_b32 s68, 0
	s_mul_i32 s30, s18, 0xd00
	s_add_u32 s30, s30, 92160
	v_add_u32_e32 v7, s30, v2
	v_mul_u32_u24_e32 v6, 0x68, v3
	v_lshrrev_b32_e32 v130, 2, v1
	v_and_b32_e32 v130, 8, v130
	v_add3_u32 v6, v6, v130, s30
	v_mov_b32_e32 v150, 0xf149f2ca
	s_waitcnt lgkmcnt(0)
	s_sub_u32 s30, s27, s25
	s_mul_i32 s30, s30, 6
	s_add_u32 s30, s30, s24
	s_mul_i32 s31, s27, 6
	s_add_u32 s31, s31, s22
	s_cmp_lt_u32 s27, s25
	s_cselect_b32 s30, s31, s30
	s_lshl_b32 s33, s18, 10
	s_lshl_b32 s31, s30, 12
	s_add_u32 s31, s31, s33
	s_add_u32 s50, s8, s31
	s_addc_u32 s51, s9, 0
	s_add_u32 s52, s50, 0x3000
	s_addc_u32 s53, s51, 0
	s_add_u32 s34, s46, s33
	s_mov_b32 m0, s34
	s_add_u32 s35, s34, 0x3000
	global_load_lds_dwordx4 v2, s[50:51]
	s_mov_b32 m0, s35
	s_nop 0
	global_load_lds_dwordx4 v2, s[52:53]
	s_cmp_lt_u32 s18, 6
	s_cbranch_scc0 .Lm_nok_p0
	s_lshl_b32 s31, s30, 10
	s_add_u32 s31, s31, s33
	s_add_u32 s54, s4, s31
	s_addc_u32 s55, s5, 0
	s_add_u32 s34, s34, 24576
	s_mov_b32 m0, s34
	s_nop 0
	global_load_lds_dwordx4 v2, s[54:55]

.Lm_steps:
	s_waitcnt lgkmcnt(4)
	v_mfma_f32_32x32x16_f16 v[64:79], v[92:95], v[8:11], 0
	ds_read_b128 v[88:91], v128 offset:26624
	s_sub_u32 s30, s28, s25
	ds_read_b128 v[112:115], v128 offset:4096
	s_mul_i32 s30, s30, 6
	ds_read_b128 v[120:123], v128 offset:6144
	s_add_u32 s30, s30, s24
	v_exp_f32_e32 v48, v48
	s_mul_i32 s31, s28, 6
	v_exp_f32_e32 v49, v49
	s_add_u32 s31, s31, s22
	v_exp_f32_e32 v50, v50
	s_cmp_lt_u32 s28, s25
	v_exp_f32_e32 v51, v51
	s_cselect_b32 s30, s31, s30
	v_exp_f32_e32 v52, v52
	s_lshl_b32 s33, s18, 10
	v_exp_f32_e32 v53, v53
	s_lshl_b32 s31, s30, 12
	v_exp_f32_e32 v54, v54
	s_add_u32 s31, s31, s33
	v_exp_f32_e32 v55, v55
	s_add_u32 s50, s8, s31
	v_cvt_pk_bf16_f32 v80, v48, v49
	s_addc_u32 s51, s9, 0
	v_cvt_pk_bf16_f32 v81, v50, v51
	s_add_u32 s52, s50, 0x3000
	v_cvt_pk_bf16_f32 v82, v52, v53
	s_addc_u32 s53, s51, 0
	v_cvt_pk_bf16_f32 v83, v54, v55
	s_lshl_b32 s31, s30, 10
	ds_read_b128 v[116:119], v128 offset:5120
	s_add_u32 s31, s31, s33
	ds_read_b128 v[124:127], v128 offset:7168
	s_add_u32 s54, s4, s31
	v_exp_f32_e32 v56, v56
	s_addc_u32 s55, s5, 0
	v_exp_f32_e32 v57, v57
	s_add_u32 s34, s48, s33
	v_exp_f32_e32 v58, v58
	s_add_u32 s35, s34, 0x3000
	v_exp_f32_e32 v59, v59
	s_add_u32 s36, s34, 24576
	s_waitcnt lgkmcnt(7)
	v_mfma_f32_32x32x16_bf16 v[16:31], v[96:99], v[80:83], v[16:31]
	v_exp_f32_e32 v60, v60
	v_exp_f32_e32 v61, v61
	v_exp_f32_e32 v62, v62
	v_exp_f32_e32 v63, v63
	v_mfma_f32_32x32x16_bf16 v[32:47], v[104:107], v[80:83], v[32:47]
	v_cvt_pk_bf16_f32 v84, v56, v57
	v_cvt_pk_bf16_f32 v85, v58, v59
	v_cvt_pk_bf16_f32 v86, v60, v61
	v_cvt_pk_bf16_f32 v87, v62, v63
.Lm_after0:
	s_cmp_lt_u32 s28, 9
	s_cbranch_scc0 .Lm_nod_lp
	s_mov_b32 m0, s34
	s_nop 0
	global_load_lds_dwordx4 v2, s[50:51]
	s_mov_b32 m0, s35
	s_nop 0
	global_load_lds_dwordx4 v2, s[52:53]
	s_cmp_lt_u32 s18, 6
	s_cbranch_scc0 .Lm_nod_lp
	s_mov_b32 m0, s36
	s_nop 0
	global_load_lds_dwordx4 v2, s[54:55]

.Lm_bar:
	s_barrier
	v_add_u32_e32 v128, s46, v2
	v_add_u32_e32 v129, s47, v2
	s_add_u32 s28, s27, 2
	s_cmp_eq_u32 s68, 1
	s_mov_b32 s68, 0
	s_cbranch_scc1 .Lm_steps_fresh
	s_branch .Lm_steps

.Lm_switch:
	v_mov_b32_e32 v8, v12
	v_mov_b32_e32 v9, v13
	v_mov_b32_e32 v10, v14
	v_mov_b32_e32 v11, v15
	v_mov_b32_e32 v148, v149
	s_add_u32 s29, s23, 0x100
	s_mov_b32 s68, 1
	v_mfma_f32_32x32x16_f16 v[48:63], v[88:91], v[8:11], 0
	s_waitcnt vmcnt(5)
	s_branch .Lm_bar
.Lm_steps_fresh:
	s_waitcnt lgkmcnt(4)
	v_mfma_f32_32x32x16_f16 v[64:79], v[92:95], v[8:11], 0
	ds_read_b128 v[88:91], v128 offset:26624
	s_sub_u32 s30, s28, s25
	ds_read_b128 v[112:115], v128 offset:4096
	s_mul_i32 s30, s30, 6
	ds_read_b128 v[120:123], v128 offset:6144
	s_add_u32 s30, s30, s24
	v_exp_f32_e32 v48, v48
	s_mul_i32 s31, s28, 6
	v_exp_f32_e32 v49, v49
	s_add_u32 s31, s31, s22
	v_exp_f32_e32 v50, v50
	s_cmp_lt_u32 s28, s25
	v_exp_f32_e32 v51, v51
	s_cselect_b32 s30, s31, s30
	v_exp_f32_e32 v52, v52
	s_lshl_b32 s33, s18, 10
	v_exp_f32_e32 v53, v53
	s_lshl_b32 s31, s30, 12
	v_exp_f32_e32 v54, v54
	s_add_u32 s31, s31, s33
	v_exp_f32_e32 v55, v55
	s_add_u32 s50, s8, s31
	v_cvt_pk_bf16_f32 v80, v48, v49
	s_addc_u32 s51, s9, 0
	v_cvt_pk_bf16_f32 v81, v50, v51
	s_add_u32 s52, s50, 0x3000
	v_cvt_pk_bf16_f32 v82, v52, v53
	s_addc_u32 s53, s51, 0
	v_cvt_pk_bf16_f32 v83, v54, v55
	s_lshl_b32 s31, s30, 10
	ds_read_b128 v[116:119], v128 offset:5120
	s_add_u32 s31, s31, s33
	ds_read_b128 v[124:127], v128 offset:7168
	s_add_u32 s54, s4, s31
	v_exp_f32_e32 v56, v56
	s_addc_u32 s55, s5, 0
	v_exp_f32_e32 v57, v57
	s_add_u32 s34, s48, s33
	v_exp_f32_e32 v58, v58
	s_add_u32 s35, s34, 0x3000
	v_exp_f32_e32 v59, v59
	s_add_u32 s36, s34, 24576
	s_waitcnt lgkmcnt(7)
	v_mfma_f32_32x32x16_bf16 v[16:31], v[96:99], v[80:83], 0
	v_exp_f32_e32 v60, v60
	v_exp_f32_e32 v61, v61
	v_exp_f32_e32 v62, v62
	v_exp_f32_e32 v63, v63
	v_mfma_f32_32x32x16_bf16 v[32:47], v[104:107], v[80:83], 0
	v_cvt_pk_bf16_f32 v84, v56, v57
	v_cvt_pk_bf16_f32 v85, v58, v59
	v_cvt_pk_bf16_f32 v86, v60, v61
	v_cvt_pk_bf16_f32 v87, v62, v63
	s_branch .Lm_after0
